# phase-1 router-weight preparation loops: all loads issued before the first wait (on top of the router top-4 rewrite)
# speedup vs baseline: 1.0110x; 1.0046x over previous
; __device__ __forceinline__ bf16_t f2bf(float f) { unsigned u = __float_as_uint(f); u += 0x7FFFu + ((u >> 16) & 1u); return (bf16_t)(u >> 16); }
; __device__ __forceinline__ float bf2f(bf16_t b) { return __uint_as_float(((unsigned)b) << 16); }
; #define MOD WSP(float, W_MOD)
; #define WRP WSP(float, W_WRP)
; __device__ __forceinline__ void wrp_phase(const float* __restrict__ norm2, const float* __restrict__ w_router, const float* __restrict__ b_router, unsigned char* ws, int G, int c) {
;     ...
;     for (int i = c * 512 + tid; i < DEPTH * NB * D * NE; i += G * 512) {
;         const int e = i & 31, k = (i >> 5) & 1023, b = (i >> 15) & 7, l = i >> 18;
;         const float sc = MOD[((size_t)l * NB + b) * 6 * D + 4 * D + k];
;         const float wv = norm2[l * D + k] * (1.f + sc) * w_router[((size_t)l * D + k) * NE + e];
;         const bf16_t hi = f2bf(wv), lo = f2bf(wv - bf2f(hi));
;         bf16_t* WH = (bf16_t*)WRP; bf16_t* WL = WH + (size_t)DEPTH * NB * D * NE;
;         const size_t wi = ((size_t)(l * NB + b) * 128 + (k >> 3)) * 256 + e * 8 + (k & 7);
;         WH[wi] = hi; WL[wi] = lo;
;     }
.LBB0_215:
	s_cmp_lt_i32 s81, 2
	s_cselect_b64 s[2:3], -1, 0
	s_and_b64 s[0:1], s[2:3], s[0:1]
	s_andn2_b64 vcc, exec, s[0:1]
	s_cbranch_vccnz .LBB0_231
	s_mov_b64 s[10:11], s[86:87]
	s_mov_b64 s[2:3], s[86:87]
	s_load_dwordx2 s[4:5], s[2:3], 0x68
	s_mov_b64 s[2:3], s[86:87]
	s_mov_b64 s[6:7], s[86:87]
	s_load_dwordx2 s[2:3], s[2:3], 0x70
	s_load_dwordx2 s[6:7], s[6:7], 0xa8
	s_waitcnt lgkmcnt(0)
	s_load_dword s20, s[86:87], 0xb8
	v_readlane_b32 s21, v254, 0
	v_mov_b32_e32 v1, v0
	s_mov_b32 s8, 0x100000
	s_waitcnt lgkmcnt(0)
	s_mov_b32 s22, s20
	s_waitcnt vmcnt(7)
	v_lshl_add_u32 v5, s21, 9, v1
	v_cmp_gt_i32_e32 vcc, s8, v5
	s_and_saveexec_b64 s[8:9], vcc
	s_cbranch_execz .LBB0_219
	s_add_u32 s12, s6, 0x1b988000
	s_load_dwordx2 s[10:11], s[10:11], 0x60
	s_addc_u32 s13, s7, 0
	s_add_u32 s14, s6, 0x1bb4c000
	s_addc_u32 s15, s7, 0
	s_add_u32 s16, s6, 0x1bd4c000
	v_and_b32_e32 v2, 31, v1
	v_mov_b32_e32 v3, 0
	s_addc_u32 s17, s7, 0
	s_lshl_b32 s23, s22, 9
	v_lshlrev_b32_e32 v4, 3, v2
	s_mov_b64 s[18:19], 0
	s_movk_i32 s24, 0x4000
	s_waitcnt vmcnt(6)
	v_lshlrev_b32_e32 v6, 2, v2
	v_mov_b32_e32 v7, v3
	s_movk_i32 s25, 0x7fff
	s_movk_i32 s26, 0x7f00
	s_mov_b32 s27, 0xfffff
	s_cmp_lg_u32 s23, 0x20000
	s_cbranch_scc1 .LBB0_218
	s_waitcnt lgkmcnt(0)
	v_mov_b32_e32 v100, v5
	v_bfe_u32 v108, v100, 15, 3
	v_ashrrev_i32_e32 v101, 18, v100
	v_bfe_u32 v102, v100, 5, 10
	v_lshl_or_b32 v103, v101, 3, v108
	v_lshl_or_b32 v109, v101, 10, v102
	v_lshlrev_b32_e32 v104, 2, v109
	v_mul_u32_u24_e32 v105, 0x6000, v103
	v_lshl_add_u32 v105, v102, 2, v105
	v_add_u32_e32 v105, 0x4000, v105
	v_lshlrev_b32_e32 v106, 17, v101
	v_lshl_add_u32 v106, v102, 7, v106
	v_add_u32_e32 v106, v106, v6
	global_load_dword v104, v104, s[10:11]
	global_load_dword v105, v105, s[12:13]
	global_load_dword v106, v106, s[4:5]
	v_lshlrev_b32_e32 v107, 15, v103
	v_and_or_b32 v107, v100, s26, v107
	v_or_b32_e32 v107, v107, v4
	v_lshrrev_b32_e32 v108, 5, v100
	v_and_or_b32 v107, v108, 7, v107
	v_lshlrev_b32_e32 v107, 1, v107
	v_add_u32_e32 v110, 0x20000, v5
	v_bfe_u32 v118, v110, 15, 3
	v_ashrrev_i32_e32 v111, 18, v110
	v_bfe_u32 v112, v110, 5, 10
	v_lshl_or_b32 v113, v111, 3, v118
	v_lshl_or_b32 v119, v111, 10, v112
	v_lshlrev_b32_e32 v114, 2, v119
	v_mul_u32_u24_e32 v115, 0x6000, v113
	v_lshl_add_u32 v115, v112, 2, v115
	v_add_u32_e32 v115, 0x4000, v115
	v_lshlrev_b32_e32 v116, 17, v111
	v_lshl_add_u32 v116, v112, 7, v116
	v_add_u32_e32 v116, v116, v6
	global_load_dword v114, v114, s[10:11]
	global_load_dword v115, v115, s[12:13]
	global_load_dword v116, v116, s[4:5]
	v_lshlrev_b32_e32 v117, 15, v113
	v_and_or_b32 v117, v110, s26, v117
	v_or_b32_e32 v117, v117, v4
	v_lshrrev_b32_e32 v118, 5, v110
	v_and_or_b32 v117, v118, 7, v117
	v_lshlrev_b32_e32 v117, 1, v117
	v_add_u32_e32 v120, 0x40000, v5
	v_bfe_u32 v128, v120, 15, 3
	v_ashrrev_i32_e32 v121, 18, v120
	v_bfe_u32 v122, v120, 5, 10
	v_lshl_or_b32 v123, v121, 3, v128
	v_lshl_or_b32 v129, v121, 10, v122
	v_lshlrev_b32_e32 v124, 2, v129
	v_mul_u32_u24_e32 v125, 0x6000, v123
	v_lshl_add_u32 v125, v122, 2, v125
	v_add_u32_e32 v125, 0x4000, v125
	v_lshlrev_b32_e32 v126, 17, v121
	v_lshl_add_u32 v126, v122, 7, v126
	v_add_u32_e32 v126, v126, v6
	global_load_dword v124, v124, s[10:11]
	global_load_dword v125, v125, s[12:13]
	global_load_dword v126, v126, s[4:5]
	v_lshlrev_b32_e32 v127, 15, v123
	v_and_or_b32 v127, v120, s26, v127
	v_or_b32_e32 v127, v127, v4
	v_lshrrev_b32_e32 v128, 5, v120
	v_and_or_b32 v127, v128, 7, v127
	v_lshlrev_b32_e32 v127, 1, v127
	v_add_u32_e32 v130, 0x60000, v5
	v_bfe_u32 v138, v130, 15, 3
	v_ashrrev_i32_e32 v131, 18, v130
	v_bfe_u32 v132, v130, 5, 10
	v_lshl_or_b32 v133, v131, 3, v138
	v_lshl_or_b32 v139, v131, 10, v132
	v_lshlrev_b32_e32 v134, 2, v139
	v_mul_u32_u24_e32 v135, 0x6000, v133
	v_lshl_add_u32 v135, v132, 2, v135
	v_add_u32_e32 v135, 0x4000, v135
	v_lshlrev_b32_e32 v136, 17, v131
	v_lshl_add_u32 v136, v132, 7, v136
	v_add_u32_e32 v136, v136, v6
	global_load_dword v134, v134, s[10:11]
	global_load_dword v135, v135, s[12:13]
	global_load_dword v136, v136, s[4:5]
	v_lshlrev_b32_e32 v137, 15, v133
	v_and_or_b32 v137, v130, s26, v137
	v_or_b32_e32 v137, v137, v4
	v_lshrrev_b32_e32 v138, 5, v130
	v_and_or_b32 v137, v138, 7, v137
	v_lshlrev_b32_e32 v137, 1, v137
	v_add_u32_e32 v140, 0x80000, v5
	v_bfe_u32 v148, v140, 15, 3
	v_ashrrev_i32_e32 v141, 18, v140
	v_bfe_u32 v142, v140, 5, 10
	v_lshl_or_b32 v143, v141, 3, v148
	v_lshl_or_b32 v149, v141, 10, v142
	v_lshlrev_b32_e32 v144, 2, v149
	v_mul_u32_u24_e32 v145, 0x6000, v143
	v_lshl_add_u32 v145, v142, 2, v145
	v_add_u32_e32 v145, 0x4000, v145
	v_lshlrev_b32_e32 v146, 17, v141
	v_lshl_add_u32 v146, v142, 7, v146
	v_add_u32_e32 v146, v146, v6
	global_load_dword v144, v144, s[10:11]
	global_load_dword v145, v145, s[12:13]
	global_load_dword v146, v146, s[4:5]
	v_lshlrev_b32_e32 v147, 15, v143
	v_and_or_b32 v147, v140, s26, v147
	v_or_b32_e32 v147, v147, v4
	v_lshrrev_b32_e32 v148, 5, v140
	v_and_or_b32 v147, v148, 7, v147
	v_lshlrev_b32_e32 v147, 1, v147
	v_add_u32_e32 v150, 0xa0000, v5
	v_bfe_u32 v158, v150, 15, 3
	v_ashrrev_i32_e32 v151, 18, v150
	v_bfe_u32 v152, v150, 5, 10
	v_lshl_or_b32 v153, v151, 3, v158
	v_lshl_or_b32 v159, v151, 10, v152
	v_lshlrev_b32_e32 v154, 2, v159
	v_mul_u32_u24_e32 v155, 0x6000, v153
; __device__ __forceinline__ bf16_t f2bf(float f) { unsigned u = __float_as_uint(f); u += 0x7FFFu + ((u >> 16) & 1u); return (bf16_t)(u >> 16); }
; __device__ __forceinline__ float bf2f(bf16_t b) { return __uint_as_float(((unsigned)b) << 16); }
; #define MOD WSP(float, W_MOD)
; #define WRP WSP(float, W_WRP)
; __device__ __forceinline__ void wrp_phase(const float* __restrict__ norm2, const float* __restrict__ w_router, const float* __restrict__ b_router, unsigned char* ws, int G, int c) {
;     ...
;     for (int i = c * 512 + tid; i < DEPTH * NB * D * NE; i += G * 512) {
;         const int e = i & 31, k = (i >> 5) & 1023, b = (i >> 15) & 7, l = i >> 18;
;         const float sc = MOD[((size_t)l * NB + b) * 6 * D + 4 * D + k];
;         const float wv = norm2[l * D + k] * (1.f + sc) * w_router[((size_t)l * D + k) * NE + e];
;         const bf16_t hi = f2bf(wv), lo = f2bf(wv - bf2f(hi));
;         bf16_t* WH = (bf16_t*)WRP; bf16_t* WL = WH + (size_t)DEPTH * NB * D * NE;
;         const size_t wi = ((size_t)(l * NB + b) * 128 + (k >> 3)) * 256 + e * 8 + (k & 7);
;         WH[wi] = hi; WL[wi] = lo;
;     }
	v_lshl_add_u32 v155, v152, 2, v155
	v_add_u32_e32 v155, 0x4000, v155
	v_lshlrev_b32_e32 v156, 17, v151
	v_lshl_add_u32 v156, v152, 7, v156
	v_add_u32_e32 v156, v156, v6
	global_load_dword v154, v154, s[10:11]
	global_load_dword v155, v155, s[12:13]
	global_load_dword v156, v156, s[4:5]
	v_lshlrev_b32_e32 v157, 15, v153
	v_and_or_b32 v157, v150, s26, v157
	v_or_b32_e32 v157, v157, v4
	v_lshrrev_b32_e32 v158, 5, v150
	v_and_or_b32 v157, v158, 7, v157
	v_lshlrev_b32_e32 v157, 1, v157
	v_add_u32_e32 v160, 0xc0000, v5
	v_bfe_u32 v168, v160, 15, 3
	v_ashrrev_i32_e32 v161, 18, v160
	v_bfe_u32 v162, v160, 5, 10
	v_lshl_or_b32 v163, v161, 3, v168
	v_lshl_or_b32 v169, v161, 10, v162
	v_lshlrev_b32_e32 v164, 2, v169
	v_mul_u32_u24_e32 v165, 0x6000, v163
	v_lshl_add_u32 v165, v162, 2, v165
	v_add_u32_e32 v165, 0x4000, v165
	v_lshlrev_b32_e32 v166, 17, v161
	v_lshl_add_u32 v166, v162, 7, v166
	v_add_u32_e32 v166, v166, v6
	global_load_dword v164, v164, s[10:11]
	global_load_dword v165, v165, s[12:13]
	global_load_dword v166, v166, s[4:5]
	v_lshlrev_b32_e32 v167, 15, v163
	v_and_or_b32 v167, v160, s26, v167
	v_or_b32_e32 v167, v167, v4
	v_lshrrev_b32_e32 v168, 5, v160
	v_and_or_b32 v167, v168, 7, v167
	v_lshlrev_b32_e32 v167, 1, v167
	v_add_u32_e32 v170, 0xe0000, v5
	v_bfe_u32 v178, v170, 15, 3
	v_ashrrev_i32_e32 v171, 18, v170
	v_bfe_u32 v172, v170, 5, 10
	v_lshl_or_b32 v173, v171, 3, v178
	v_lshl_or_b32 v179, v171, 10, v172
	v_lshlrev_b32_e32 v174, 2, v179
	v_mul_u32_u24_e32 v175, 0x6000, v173
	v_lshl_add_u32 v175, v172, 2, v175
	v_add_u32_e32 v175, 0x4000, v175
	v_lshlrev_b32_e32 v176, 17, v171
	v_lshl_add_u32 v176, v172, 7, v176
	v_add_u32_e32 v176, v176, v6
	global_load_dword v174, v174, s[10:11]
	global_load_dword v175, v175, s[12:13]
	global_load_dword v176, v176, s[4:5]
	v_lshlrev_b32_e32 v177, 15, v173
	v_and_or_b32 v177, v170, s26, v177
	v_or_b32_e32 v177, v177, v4
	v_lshrrev_b32_e32 v178, 5, v170
	v_and_or_b32 v177, v178, 7, v177
	v_lshlrev_b32_e32 v177, 1, v177
	s_waitcnt vmcnt(21)
	v_add_f32_e32 v105, 1.0, v105
	v_mul_f32_e32 v105, v104, v105
	v_mul_f32_e32 v100, v105, v106
	v_bfe_u32 v108, v100, 16, 1
	v_add3_u32 v100, v100, v108, s25
	v_and_b32_e32 v108, 0xffff0000, v100
	v_fma_f32 v105, v105, v106, -v108
	global_store_short_d16_hi v107, v100, s[14:15]
	v_bfe_u32 v108, v105, 16, 1
	v_add3_u32 v105, v105, v108, s25
	global_store_short_d16_hi v107, v105, s[16:17]
	s_waitcnt vmcnt(20)
	v_add_f32_e32 v115, 1.0, v115
	v_mul_f32_e32 v115, v114, v115
	v_mul_f32_e32 v110, v115, v116
	v_bfe_u32 v118, v110, 16, 1
	v_add3_u32 v110, v110, v118, s25
	v_and_b32_e32 v118, 0xffff0000, v110
	v_fma_f32 v115, v115, v116, -v118
	global_store_short_d16_hi v117, v110, s[14:15]
	v_bfe_u32 v118, v115, 16, 1
	v_add3_u32 v115, v115, v118, s25
	global_store_short_d16_hi v117, v115, s[16:17]
	s_waitcnt vmcnt(19)
	v_add_f32_e32 v125, 1.0, v125
	v_mul_f32_e32 v125, v124, v125
	v_mul_f32_e32 v120, v125, v126
	v_bfe_u32 v128, v120, 16, 1
	v_add3_u32 v120, v120, v128, s25
	v_and_b32_e32 v128, 0xffff0000, v120
	v_fma_f32 v125, v125, v126, -v128
	global_store_short_d16_hi v127, v120, s[14:15]
	v_bfe_u32 v128, v125, 16, 1
	v_add3_u32 v125, v125, v128, s25
	global_store_short_d16_hi v127, v125, s[16:17]
	s_waitcnt vmcnt(18)
	v_add_f32_e32 v135, 1.0, v135
	v_mul_f32_e32 v135, v134, v135
	v_mul_f32_e32 v130, v135, v136
	v_bfe_u32 v138, v130, 16, 1
	v_add3_u32 v130, v130, v138, s25
	v_and_b32_e32 v138, 0xffff0000, v130
	v_fma_f32 v135, v135, v136, -v138
	global_store_short_d16_hi v137, v130, s[14:15]
	v_bfe_u32 v138, v135, 16, 1
	v_add3_u32 v135, v135, v138, s25
	global_store_short_d16_hi v137, v135, s[16:17]
	s_waitcnt vmcnt(17)
	v_add_f32_e32 v145, 1.0, v145
	v_mul_f32_e32 v145, v144, v145
	v_mul_f32_e32 v140, v145, v146
	v_bfe_u32 v148, v140, 16, 1
	v_add3_u32 v140, v140, v148, s25
	v_and_b32_e32 v148, 0xffff0000, v140
	v_fma_f32 v145, v145, v146, -v148
	global_store_short_d16_hi v147, v140, s[14:15]
	v_bfe_u32 v148, v145, 16, 1
	v_add3_u32 v145, v145, v148, s25
	global_store_short_d16_hi v147, v145, s[16:17]
	s_waitcnt vmcnt(16)
	v_add_f32_e32 v155, 1.0, v155
	v_mul_f32_e32 v155, v154, v155
	v_mul_f32_e32 v150, v155, v156
	v_bfe_u32 v158, v150, 16, 1
	v_add3_u32 v150, v150, v158, s25
	v_and_b32_e32 v158, 0xffff0000, v150
	v_fma_f32 v155, v155, v156, -v158
	global_store_short_d16_hi v157, v150, s[14:15]
	v_bfe_u32 v158, v155, 16, 1
	v_add3_u32 v155, v155, v158, s25
	global_store_short_d16_hi v157, v155, s[16:17]
	s_waitcnt vmcnt(15)
	v_add_f32_e32 v165, 1.0, v165
	v_mul_f32_e32 v165, v164, v165
	v_mul_f32_e32 v160, v165, v166
	v_bfe_u32 v168, v160, 16, 1
	v_add3_u32 v160, v160, v168, s25
	v_and_b32_e32 v168, 0xffff0000, v160
	v_fma_f32 v165, v165, v166, -v168
	global_store_short_d16_hi v167, v160, s[14:15]
	v_bfe_u32 v168, v165, 16, 1
	v_add3_u32 v165, v165, v168, s25
	global_store_short_d16_hi v167, v165, s[16:17]
	s_waitcnt vmcnt(14)
	v_add_f32_e32 v175, 1.0, v175
	v_mul_f32_e32 v175, v174, v175
	v_mul_f32_e32 v170, v175, v176
	v_bfe_u32 v178, v170, 16, 1
	v_add3_u32 v170, v170, v178, s25
	v_and_b32_e32 v178, 0xffff0000, v170
	v_fma_f32 v175, v175, v176, -v178
	global_store_short_d16_hi v177, v170, s[14:15]
	v_bfe_u32 v178, v175, 16, 1
	v_add3_u32 v175, v175, v178, s25
	global_store_short_d16_hi v177, v175, s[16:17]
	s_branch .LBB0_219

; __device__ __forceinline__ float shx(float v, int m) { int ln; asm volatile("v_mbcnt_lo_u32_b32 %0, -1, 0\n\tv_mbcnt_hi_u32_b32 %0, -1, %0" : "=v"(ln)); return __builtin_bit_cast(float, __builtin_amdgcn_ds_bpermute((ln ^ m) << 2, __builtin_bit_cast(int, v))); }
; #define MOD WSP(float, W_MOD)
; #define BRP WSP(float, W_BRP)
; __device__ __forceinline__ void wrp_phase(const float* __restrict__ norm2, const float* __restrict__ w_router, const float* __restrict__ b_router, unsigned char* ws, int G, int c) {
;     ...
;     for (int o = c * 8 + wid; o < DEPTH * NB * NE; o += G * 8) {
;         const int e = o & 31, b = (o >> 5) & 7, l = o >> 8;
;         float s = 0.f;
;         for (int k = lane; k < D; k += 64) s += MOD[((size_t)l * NB + b) * 6 * D + 3 * D + k] * w_router[((size_t)l * D + k) * NE + e];
;         for (int of = 32; of > 0; of >>= 1) s += shx(s, of);
;         if (lane == 0) BRP[o] = s + b_router[l * NE + e];
;     }
.LBB0_223:
	global_load_dword v100, v[10:11], off
	global_load_dword v116, v[12:13], off
	v_lshl_add_u64 v[134:135], v[12:13], 0, s[14:15]
	global_load_dword v101, v[10:11], off offset:256
	global_load_dword v117, v[134:135], off
	v_lshl_add_u64 v[136:137], v[134:135], 0, s[14:15]
	global_load_dword v102, v[10:11], off offset:512
	global_load_dword v118, v[136:137], off
	v_lshl_add_u64 v[138:139], v[136:137], 0, s[14:15]
	global_load_dword v103, v[10:11], off offset:768
	global_load_dword v119, v[138:139], off
	v_lshl_add_u64 v[140:141], v[138:139], 0, s[14:15]
	global_load_dword v104, v[10:11], off offset:1024
	global_load_dword v120, v[140:141], off
	v_lshl_add_u64 v[142:143], v[140:141], 0, s[14:15]
	global_load_dword v105, v[10:11], off offset:1280
	global_load_dword v121, v[142:143], off
	v_lshl_add_u64 v[144:145], v[142:143], 0, s[14:15]
	global_load_dword v106, v[10:11], off offset:1536
	global_load_dword v122, v[144:145], off
	v_lshl_add_u64 v[146:147], v[144:145], 0, s[14:15]
	global_load_dword v107, v[10:11], off offset:1792
	global_load_dword v123, v[146:147], off
	v_lshl_add_u64 v[148:149], v[146:147], 0, s[14:15]
	global_load_dword v108, v[10:11], off offset:2048
	global_load_dword v124, v[148:149], off
	v_lshl_add_u64 v[150:151], v[148:149], 0, s[14:15]
	global_load_dword v109, v[10:11], off offset:2304
	global_load_dword v125, v[150:151], off
	v_lshl_add_u64 v[152:153], v[150:151], 0, s[14:15]
	global_load_dword v110, v[10:11], off offset:2560
	global_load_dword v126, v[152:153], off
	v_lshl_add_u64 v[154:155], v[152:153], 0, s[14:15]
	global_load_dword v111, v[10:11], off offset:2816
	global_load_dword v127, v[154:155], off
	v_lshl_add_u64 v[156:157], v[154:155], 0, s[14:15]
	global_load_dword v112, v[10:11], off offset:3072
	global_load_dword v128, v[156:157], off
	v_lshl_add_u64 v[158:159], v[156:157], 0, s[14:15]
	global_load_dword v113, v[10:11], off offset:3328
	global_load_dword v129, v[158:159], off
	v_lshl_add_u64 v[160:161], v[158:159], 0, s[14:15]
	global_load_dword v114, v[10:11], off offset:3584
	global_load_dword v130, v[160:161], off
	v_lshl_add_u64 v[162:163], v[160:161], 0, s[14:15]
	global_load_dword v115, v[10:11], off offset:3840
	global_load_dword v131, v[162:163], off
	s_waitcnt vmcnt(30)
	v_fmac_f32_e32 v3, v100, v116
	s_waitcnt vmcnt(28)
	v_fmac_f32_e32 v3, v101, v117
	s_waitcnt vmcnt(26)
	v_fmac_f32_e32 v3, v102, v118
	s_waitcnt vmcnt(24)
	v_fmac_f32_e32 v3, v103, v119
	s_waitcnt vmcnt(22)
	v_fmac_f32_e32 v3, v104, v120
	s_waitcnt vmcnt(20)
	v_fmac_f32_e32 v3, v105, v121
	s_waitcnt vmcnt(18)
	v_fmac_f32_e32 v3, v106, v122
	s_waitcnt vmcnt(16)
	v_fmac_f32_e32 v3, v107, v123
	s_waitcnt vmcnt(14)
	v_fmac_f32_e32 v3, v108, v124
	s_waitcnt vmcnt(12)
	v_fmac_f32_e32 v3, v109, v125
	s_waitcnt vmcnt(10)
	v_fmac_f32_e32 v3, v110, v126
	s_waitcnt vmcnt(8)
	v_fmac_f32_e32 v3, v111, v127
	s_waitcnt vmcnt(6)
	v_fmac_f32_e32 v3, v112, v128
	s_waitcnt vmcnt(4)
	v_fmac_f32_e32 v3, v113, v129
	s_waitcnt vmcnt(2)
	v_fmac_f32_e32 v3, v114, v130
	s_waitcnt vmcnt(0)
	v_fmac_f32_e32 v3, v115, v131
	s_or_b64 exec, exec, s[16:17]
	v_mbcnt_lo_u32_b32 v9, -1, 0
	v_mbcnt_hi_u32_b32 v9, -1, v9
	v_mbcnt_lo_u32_b32 v10, -1, 0
	v_mbcnt_hi_u32_b32 v10, -1, v10
	s_nop 0
	v_lshlrev_b32_e32 v9, 2, v9
	v_xor_b32_e32 v9, 0x80, v9
	ds_bpermute_b32 v9, v9, v3
	v_lshlrev_b32_e32 v10, 2, v10
	v_xor_b32_e32 v10, 64, v10
	s_waitcnt lgkmcnt(0)
	v_add_f32_e32 v3, v3, v9
	ds_bpermute_b32 v9, v10, v3
	v_mbcnt_lo_u32_b32 v10, -1, 0
	v_mbcnt_hi_u32_b32 v10, -1, v10
	s_waitcnt lgkmcnt(0)
	v_add_f32_e32 v3, v3, v9
	v_lshlrev_b32_e32 v10, 2, v10
	v_xor_b32_e32 v10, 32, v10
	ds_bpermute_b32 v9, v10, v3
	v_mbcnt_lo_u32_b32 v10, -1, 0
	v_mbcnt_hi_u32_b32 v10, -1, v10
	s_waitcnt lgkmcnt(0)
	v_add_f32_e32 v3, v3, v9
	v_lshlrev_b32_e32 v10, 2, v10
	v_xor_b32_e32 v10, 16, v10
	ds_bpermute_b32 v9, v10, v3
	v_mbcnt_lo_u32_b32 v10, -1, 0
	v_mbcnt_hi_u32_b32 v10, -1, v10
	s_waitcnt lgkmcnt(0)
	v_add_f32_e32 v3, v3, v9
	v_lshlrev_b32_e32 v10, 2, v10
	v_xor_b32_e32 v10, 8, v10
	ds_bpermute_b32 v9, v10, v3
	v_mbcnt_lo_u32_b32 v10, -1, 0
	v_mbcnt_hi_u32_b32 v10, -1, v10
	s_waitcnt lgkmcnt(0)
	v_add_f32_e32 v3, v3, v9
	v_lshlrev_b32_e32 v10, 2, v10
	v_xor_b32_e32 v9, 4, v10
	ds_bpermute_b32 v9, v9, v3
	s_and_saveexec_b64 s[4:5], vcc
	s_cbranch_execz .LBB0_221
	v_and_b32_e32 v10, 31, v2
	v_lshl_or_b32 v10, v8, 5, v10
	v_ashrrev_i32_e32 v11, 31, v10
	v_lshl_add_u64 v[10:11], v[10:11], 2, s[2:3]
	global_load_dword v10, v[10:11], off
	s_waitcnt lgkmcnt(0)
	v_add_f32_e32 v11, v3, v9
	v_ashrrev_i32_e32 v3, 31, v2
	v_lshl_add_u64 v[8:9], v[2:3], 2, s[10:11]
	s_waitcnt vmcnt(0)
	v_add_f32_e32 v3, v11, v10
	global_store_dword v[8:9], v3, off
	s_branch .LBB0_221
